# stack: prologue barrier replaced by adaLN-ready flag; XCD generation word signalled before the leader L1 invalidate; final grid barrier of the last layer skipped
# baseline (speedup 1.0000x reference)
; #define GRID_BAR() do { XcdBarrier _b = bar; asm volatile("" : "+s"(_b.bar), "+s"(_b.x)); refresh(F); xcd_barrier(_b, F.tid == 0); } while (0)
; __global__ void __launch_bounds__(512, 2) fwd_kernel(Args args) {
;     ...
;     for (int l = 0; l < DEPTH; ++l) {
;     ...
;         GRID_BAR();
;         phase_n2(F, l);
;         GRID_BAR();
.LBB0_1438:
	v_readlane_b32 s100, v253, 23
	v_readlane_b32 s101, v253, 24
	s_nop 3
	s_cmp_lg_u64 s[100:101], 0
	s_cbranch_scc1 .LBB0_1483
	v_readlane_b32 s2, v253, 2
	s_mov_b32 s0, s94
	v_readlane_b32 s3, v253, 3
	s_mov_b32 s1, -1
	v_readlane_b32 s4, v253, 29
	v_mbcnt_lo_u32_b32 v0, s1, 0
	v_mbcnt_hi_u32_b32 v0, s1, v0
	s_mov_b32 s39, s4
	s_lshl_b32 s1, s97, 6
	s_waitcnt vmcnt(0)
	s_sub_i32 s1, 0, s1
	v_cmp_eq_u32_e32 vcc, s1, v0
	v_readlane_b32 s5, v253, 30
	s_barrier
	s_and_saveexec_b64 s[36:37], vcc
	s_cbranch_execnz .LBB0_1439
	s_getpc_b64 s[98:99]
